# gate/up GEMM: the pair of barriers that re-aligned the two wave halves around each epilogue dropped for units with a successor (epilogues staggered by one MFMA segment); last unit keeps its aligning b
# baseline (speedup 1.0000x reference)
.LBB0_1109:
	s_and_b64 vcc, exec, s[12:13]
	s_andn2_b64 vcc, vcc, s[28:29]
	s_cbranch_vccz .LBB0_1111
	s_barrier
.LBB0_1111:
	v_pk_mul_f32 v[0:1], v[156:157], s[14:15] op_sel_hi:[1,0]
	v_pk_mul_f32 v[10:11], v[158:159], s[14:15] op_sel_hi:[1,0]
	v_exp_f32_e32 v2, v0
	v_exp_f32_e32 v3, v1
	v_exp_f32_e32 v10, v10
	v_exp_f32_e32 v11, v11
	v_pk_mul_f32 v[8:9], v[156:157], v[152:153]
	v_pk_fma_f32 v[2:3], v[2:3], s[16:17], s[16:17] op_sel_hi:[1,0,0]
	v_pk_mul_f32 v[6:7], v[158:159], v[154:155]
	v_rcp_f32_e32 v2, v2
	v_rcp_f32_e32 v3, v3
	s_mul_hi_i32 s0, s33, 0x2e8ba2e9
	s_lshr_b32 s1, s0, 31
	s_lshr_b32 s0, s0, 2
	v_pk_mul_f32 v[2:3], v[8:9], v[2:3]
	v_pk_mul_f32 v[8:9], v[148:149], s[14:15] op_sel_hi:[1,0]
	v_med3_f32 v5, v2, s49, v195
	v_med3_f32 v12, v3, s49, v195
	v_pk_fma_f32 v[2:3], v[10:11], s[16:17], s[16:17] op_sel_hi:[1,0,0]
	v_exp_f32_e32 v8, v8
	v_rcp_f32_e32 v2, v2
	v_rcp_f32_e32 v3, v3
	v_exp_f32_e32 v9, v9
	v_pk_mul_f32 v[10:11], v[148:149], v[144:145]
	s_add_i32 s0, s0, s1
	v_pk_mul_f32 v[2:3], v[6:7], v[2:3]
	v_pk_mul_f32 v[6:7], v[150:151], s[14:15] op_sel_hi:[1,0]
	v_med3_f32 v13, v2, s49, v195
	v_exp_f32_e32 v6, v6
	v_exp_f32_e32 v7, v7
	v_med3_f32 v14, v3, s49, v195
	v_pk_fma_f32 v[2:3], v[8:9], s[16:17], s[16:17] op_sel_hi:[1,0,0]
	v_pk_mul_f32 v[8:9], v[150:151], v[146:147]
	v_rcp_f32_e32 v2, v2
	v_rcp_f32_e32 v3, v3
	v_pk_fma_f32 v[6:7], v[6:7], s[16:17], s[16:17] op_sel_hi:[1,0,0]
	s_mul_i32 s0, s0, 22
	v_rcp_f32_e32 v6, v6
	v_rcp_f32_e32 v7, v7
	v_pk_mul_f32 v[2:3], v[10:11], v[2:3]
	s_sub_i32 s0, s33, s0
	v_med3_f32 v10, v2, s49, v195
	v_med3_f32 v11, v3, s49, v195
	v_pk_mul_f32 v[2:3], v[8:9], v[6:7]
	v_mov_b32_e32 v6, v161
	v_mov_b32_e32 v7, v161
	v_cvt_pk_fp8_f32 v6, v5, v12
	v_cvt_pk_fp8_f32 v7, v10, v11
	v_med3_f32 v2, v2, s49, v195
	v_med3_f32 v3, v3, s49, v195
	v_pk_mul_f32 v[8:9], v[140:141], s[14:15] op_sel_hi:[1,0]
	v_cvt_pk_fp8_f32 v6, v13, v14 op_sel:[0,0,1]
	v_cvt_pk_fp8_f32 v7, v2, v3 op_sel:[0,0,1]
	v_exp_f32_e32 v8, v8
	v_exp_f32_e32 v9, v9
	v_lshl_add_u32 v4, s26, 8, v171
	v_lshl_or_b32 v0, s0, 7, v193
	v_mov_b64_e32 v[2:3], s[6:7]
	v_ashrrev_i32_e32 v1, 31, v0
	v_mad_i64_i32 v[10:11], s[0:1], v4, s44, v[2:3]
	v_lshl_add_u64 v[10:11], v[10:11], 0, v[0:1]
	s_nop 15
	s_nop 15
	global_store_dwordx2 v[10:11], v[6:7], off
	v_pk_fma_f32 v[6:7], v[8:9], s[16:17], s[16:17] op_sel_hi:[1,0,0]
	v_pk_mul_f32 v[12:13], v[142:143], s[14:15] op_sel_hi:[1,0]
	v_rcp_f32_e32 v6, v6
	v_rcp_f32_e32 v7, v7
	v_exp_f32_e32 v12, v12
	v_exp_f32_e32 v13, v13
	v_pk_mul_f32 v[10:11], v[140:141], v[136:137]
	v_pk_mul_f32 v[8:9], v[142:143], v[138:139]
	v_pk_mul_f32 v[6:7], v[10:11], v[6:7]
	v_pk_mul_f32 v[10:11], v[132:133], s[14:15] op_sel_hi:[1,0]
	v_med3_f32 v5, v6, s49, v195
	v_med3_f32 v14, v7, s49, v195
	v_pk_fma_f32 v[6:7], v[12:13], s[16:17], s[16:17] op_sel_hi:[1,0,0]
	v_exp_f32_e32 v10, v10
	v_rcp_f32_e32 v6, v6
	v_rcp_f32_e32 v7, v7
	v_exp_f32_e32 v11, v11
	v_pk_mul_f32 v[12:13], v[132:133], v[128:129]
	s_andn2_b64 vcc, exec, s[28:29]
	v_pk_mul_f32 v[6:7], v[8:9], v[6:7]
	v_pk_mul_f32 v[8:9], v[134:135], s[14:15] op_sel_hi:[1,0]
	v_med3_f32 v15, v6, s49, v195
	v_exp_f32_e32 v8, v8
	v_exp_f32_e32 v9, v9
	v_med3_f32 v16, v7, s49, v195
	v_pk_fma_f32 v[6:7], v[10:11], s[16:17], s[16:17] op_sel_hi:[1,0,0]
	v_pk_mul_f32 v[10:11], v[134:135], v[130:131]
	v_rcp_f32_e32 v6, v6
	v_rcp_f32_e32 v7, v7
	v_pk_fma_f32 v[8:9], v[8:9], s[16:17], s[16:17] op_sel_hi:[1,0,0]
	v_pk_mul_f32 v[6:7], v[12:13], v[6:7]
	v_rcp_f32_e32 v8, v8
	v_rcp_f32_e32 v9, v9
	v_med3_f32 v12, v6, s49, v195
	v_med3_f32 v13, v7, s49, v195
	v_pk_mul_f32 v[6:7], v[10:11], v[8:9]
	v_mov_b32_e32 v9, v161
	v_cvt_pk_fp8_f32 v9, v12, v13
	v_mov_b32_e32 v8, v161
	v_cvt_pk_fp8_f32 v8, v5, v14
	v_med3_f32 v5, v6, s49, v195
	v_med3_f32 v6, v7, s49, v195
	v_cvt_pk_fp8_f32 v9, v5, v6 op_sel:[0,0,1]
	v_pk_mul_f32 v[6:7], v[124:125], s[14:15] op_sel_hi:[1,0]
	v_cvt_pk_fp8_f32 v8, v15, v16 op_sel:[0,0,1]
	v_exp_f32_e32 v6, v6
	v_exp_f32_e32 v7, v7
	v_or_b32_e32 v5, 16, v4
	v_pk_mul_f32 v[12:13], v[126:127], s[14:15] op_sel_hi:[1,0]
	v_mad_i64_i32 v[10:11], s[0:1], v5, s44, v[2:3]
	v_pk_fma_f32 v[6:7], v[6:7], s[16:17], s[16:17] op_sel_hi:[1,0,0]
	v_exp_f32_e32 v12, v12
	v_rcp_f32_e32 v6, v6
	v_rcp_f32_e32 v7, v7
	v_exp_f32_e32 v13, v13
	v_lshl_add_u64 v[10:11], v[10:11], 0, v[0:1]
	global_store_dwordx2 v[10:11], v[8:9], off
	v_pk_mul_f32 v[10:11], v[124:125], v[120:121]
	v_pk_mul_f32 v[8:9], v[126:127], v[122:123]
	v_pk_mul_f32 v[6:7], v[10:11], v[6:7]
	v_pk_mul_f32 v[10:11], v[116:117], s[14:15] op_sel_hi:[1,0]
	v_med3_f32 v5, v6, s49, v195
	v_med3_f32 v14, v7, s49, v195
	v_pk_fma_f32 v[6:7], v[12:13], s[16:17], s[16:17] op_sel_hi:[1,0,0]
	v_exp_f32_e32 v10, v10
	v_rcp_f32_e32 v6, v6
	v_rcp_f32_e32 v7, v7
	v_exp_f32_e32 v11, v11
	v_pk_mul_f32 v[12:13], v[116:117], v[112:113]
	v_pk_mul_f32 v[6:7], v[8:9], v[6:7]
	v_pk_mul_f32 v[8:9], v[118:119], s[14:15] op_sel_hi:[1,0]
	v_med3_f32 v15, v6, s49, v195
	v_exp_f32_e32 v8, v8
	v_exp_f32_e32 v9, v9
	v_med3_f32 v16, v7, s49, v195
	v_pk_fma_f32 v[6:7], v[10:11], s[16:17], s[16:17] op_sel_hi:[1,0,0]
	v_pk_mul_f32 v[10:11], v[118:119], v[114:115]
	v_rcp_f32_e32 v6, v6
	v_rcp_f32_e32 v7, v7
	v_pk_fma_f32 v[8:9], v[8:9], s[16:17], s[16:17] op_sel_hi:[1,0,0]
	v_pk_mul_f32 v[6:7], v[12:13], v[6:7]
	v_rcp_f32_e32 v8, v8
	v_rcp_f32_e32 v9, v9
	v_med3_f32 v12, v6, s49, v195
	v_med3_f32 v13, v7, s49, v195
	v_pk_mul_f32 v[6:7], v[10:11], v[8:9]
	v_mov_b32_e32 v9, v161
	v_cvt_pk_fp8_f32 v9, v12, v13
	v_mov_b32_e32 v8, v161
	v_cvt_pk_fp8_f32 v8, v5, v14
	v_med3_f32 v5, v6, s49, v195
	v_med3_f32 v6, v7, s49, v195
	v_cvt_pk_fp8_f32 v9, v5, v6 op_sel:[0,0,1]
	v_pk_mul_f32 v[6:7], v[108:109], s[14:15] op_sel_hi:[1,0]
	v_cvt_pk_fp8_f32 v8, v15, v16 op_sel:[0,0,1]
	v_exp_f32_e32 v6, v6
	v_exp_f32_e32 v7, v7
	v_or_b32_e32 v5, 32, v4
	v_pk_mul_f32 v[12:13], v[110:111], s[14:15] op_sel_hi:[1,0]
	v_mad_i64_i32 v[10:11], s[0:1], v5, s44, v[2:3]
	v_pk_fma_f32 v[6:7], v[6:7], s[16:17], s[16:17] op_sel_hi:[1,0,0]
	v_exp_f32_e32 v12, v12
	v_rcp_f32_e32 v6, v6
	v_rcp_f32_e32 v7, v7
	v_exp_f32_e32 v13, v13
	v_lshl_add_u64 v[10:11], v[10:11], 0, v[0:1]
	global_store_dwordx2 v[10:11], v[8:9], off
	v_pk_mul_f32 v[10:11], v[108:109], v[104:105]
	v_pk_mul_f32 v[8:9], v[110:111], v[106:107]
	v_pk_mul_f32 v[6:7], v[10:11], v[6:7]
	v_pk_mul_f32 v[10:11], v[100:101], s[14:15] op_sel_hi:[1,0]
	v_med3_f32 v5, v6, s49, v195
	v_med3_f32 v14, v7, s49, v195
	v_pk_fma_f32 v[6:7], v[12:13], s[16:17], s[16:17] op_sel_hi:[1,0,0]
	v_exp_f32_e32 v10, v10
	v_rcp_f32_e32 v6, v6
	v_rcp_f32_e32 v7, v7
	v_exp_f32_e32 v11, v11
	v_pk_mul_f32 v[12:13], v[100:101], v[96:97]
	v_pk_mul_f32 v[6:7], v[8:9], v[6:7]
	v_pk_mul_f32 v[8:9], v[102:103], s[14:15] op_sel_hi:[1,0]
	v_med3_f32 v15, v6, s49, v195
	v_exp_f32_e32 v8, v8
	v_exp_f32_e32 v9, v9
	v_med3_f32 v16, v7, s49, v195
	v_pk_fma_f32 v[6:7], v[10:11], s[16:17], s[16:17] op_sel_hi:[1,0,0]
	v_pk_mul_f32 v[10:11], v[102:103], v[98:99]
	v_rcp_f32_e32 v6, v6
	v_rcp_f32_e32 v7, v7
	v_pk_fma_f32 v[8:9], v[8:9], s[16:17], s[16:17] op_sel_hi:[1,0,0]
	v_pk_mul_f32 v[6:7], v[12:13], v[6:7]
	v_rcp_f32_e32 v8, v8
	v_rcp_f32_e32 v9, v9
	v_med3_f32 v12, v6, s49, v195
	v_med3_f32 v13, v7, s49, v195
	v_pk_mul_f32 v[6:7], v[10:11], v[8:9]
	v_mov_b32_e32 v8, v161
	v_mov_b32_e32 v9, v161
	v_cvt_pk_fp8_f32 v8, v5, v14
	v_cvt_pk_fp8_f32 v9, v12, v13
	v_med3_f32 v5, v6, s49, v195
	v_med3_f32 v6, v7, s49, v195
	v_pk_mul_f32 v[10:11], v[92:93], s[14:15] op_sel_hi:[1,0]
	v_cvt_pk_fp8_f32 v8, v15, v16 op_sel:[0,0,1]
	v_cvt_pk_fp8_f32 v9, v5, v6 op_sel:[0,0,1]
	v_exp_f32_e32 v10, v10
	v_exp_f32_e32 v11, v11
	v_or_b32_e32 v5, 48, v4
	v_mad_i64_i32 v[6:7], s[0:1], v5, s44, v[2:3]
	v_lshl_add_u64 v[6:7], v[6:7], 0, v[0:1]
	global_store_dwordx2 v[6:7], v[8:9], off
	v_pk_fma_f32 v[6:7], v[10:11], s[16:17], s[16:17] op_sel_hi:[1,0,0]
	v_pk_mul_f32 v[12:13], v[94:95], s[14:15] op_sel_hi:[1,0]
	v_rcp_f32_e32 v6, v6
	v_rcp_f32_e32 v7, v7
	v_exp_f32_e32 v12, v12
	v_exp_f32_e32 v13, v13
	v_pk_mul_f32 v[10:11], v[92:93], v[88:89]
	v_pk_mul_f32 v[8:9], v[94:95], v[90:91]
	v_pk_mul_f32 v[6:7], v[10:11], v[6:7]
	v_pk_mul_f32 v[10:11], v[84:85], s[14:15] op_sel_hi:[1,0]
	v_med3_f32 v14, v6, s49, v195
	v_med3_f32 v15, v7, s49, v195
	v_pk_fma_f32 v[6:7], v[12:13], s[16:17], s[16:17] op_sel_hi:[1,0,0]
	v_exp_f32_e32 v10, v10
	v_rcp_f32_e32 v6, v6
	v_rcp_f32_e32 v7, v7
	v_exp_f32_e32 v11, v11
	v_pk_mul_f32 v[12:13], v[84:85], v[80:81]
	v_add_u32_e32 v5, 0x80, v4
	v_pk_mul_f32 v[6:7], v[8:9], v[6:7]
	v_pk_mul_f32 v[8:9], v[86:87], s[14:15] op_sel_hi:[1,0]
	v_med3_f32 v16, v6, s49, v195
	v_exp_f32_e32 v8, v8
	v_exp_f32_e32 v9, v9
	v_med3_f32 v17, v7, s49, v195
	v_pk_fma_f32 v[6:7], v[10:11], s[16:17], s[16:17] op_sel_hi:[1,0,0]
	v_pk_mul_f32 v[10:11], v[86:87], v[82:83]
	v_rcp_f32_e32 v6, v6
	v_rcp_f32_e32 v7, v7
	v_pk_fma_f32 v[8:9], v[8:9], s[16:17], s[16:17] op_sel_hi:[1,0,0]
	v_pk_mul_f32 v[6:7], v[12:13], v[6:7]
	v_rcp_f32_e32 v8, v8
	v_rcp_f32_e32 v9, v9
	v_med3_f32 v12, v6, s49, v195
	v_med3_f32 v13, v7, s49, v195
	v_pk_mul_f32 v[6:7], v[10:11], v[8:9]
	v_mov_b32_e32 v9, v161
	v_cvt_pk_fp8_f32 v9, v12, v13
	v_med3_f32 v6, v6, s49, v195
	v_med3_f32 v7, v7, s49, v195
	v_mov_b32_e32 v8, v161
	v_cvt_pk_fp8_f32 v9, v6, v7 op_sel:[0,0,1]
	v_pk_mul_f32 v[6:7], v[76:77], s[14:15] op_sel_hi:[1,0]
	v_cvt_pk_fp8_f32 v8, v14, v15
	v_exp_f32_e32 v6, v6
	v_exp_f32_e32 v7, v7
	v_pk_mul_f32 v[12:13], v[78:79], s[14:15] op_sel_hi:[1,0]
	v_cvt_pk_fp8_f32 v8, v16, v17 op_sel:[0,0,1]
	v_mad_i64_i32 v[10:11], s[0:1], v5, s44, v[2:3]
	v_pk_fma_f32 v[6:7], v[6:7], s[16:17], s[16:17] op_sel_hi:[1,0,0]
	v_exp_f32_e32 v12, v12
	v_rcp_f32_e32 v6, v6
	v_rcp_f32_e32 v7, v7
	v_exp_f32_e32 v13, v13
	v_lshl_add_u64 v[10:11], v[10:11], 0, v[0:1]
	global_store_dwordx2 v[10:11], v[8:9], off
	v_pk_mul_f32 v[10:11], v[76:77], v[72:73]
	v_pk_mul_f32 v[8:9], v[78:79], v[74:75]
	v_pk_mul_f32 v[6:7], v[10:11], v[6:7]
	v_pk_mul_f32 v[10:11], v[68:69], s[14:15] op_sel_hi:[1,0]
	v_med3_f32 v5, v6, s49, v195
	v_med3_f32 v14, v7, s49, v195
	v_pk_fma_f32 v[6:7], v[12:13], s[16:17], s[16:17] op_sel_hi:[1,0,0]
	v_exp_f32_e32 v10, v10
	v_rcp_f32_e32 v6, v6
	v_rcp_f32_e32 v7, v7
	v_exp_f32_e32 v11, v11
	v_pk_mul_f32 v[12:13], v[68:69], v[64:65]
	v_pk_mul_f32 v[6:7], v[8:9], v[6:7]
	v_pk_mul_f32 v[8:9], v[70:71], s[14:15] op_sel_hi:[1,0]
	v_med3_f32 v15, v6, s49, v195
	v_exp_f32_e32 v8, v8
	v_exp_f32_e32 v9, v9
	v_med3_f32 v16, v7, s49, v195
	v_pk_fma_f32 v[6:7], v[10:11], s[16:17], s[16:17] op_sel_hi:[1,0,0]
	v_pk_mul_f32 v[10:11], v[70:71], v[66:67]
	v_rcp_f32_e32 v6, v6
	v_rcp_f32_e32 v7, v7
	v_pk_fma_f32 v[8:9], v[8:9], s[16:17], s[16:17] op_sel_hi:[1,0,0]
	v_pk_mul_f32 v[6:7], v[12:13], v[6:7]
	v_rcp_f32_e32 v8, v8
	v_rcp_f32_e32 v9, v9
	v_med3_f32 v12, v6, s49, v195
	v_med3_f32 v13, v7, s49, v195
	v_pk_mul_f32 v[6:7], v[10:11], v[8:9]
	v_mov_b32_e32 v9, v161
	v_cvt_pk_fp8_f32 v9, v12, v13
	v_mov_b32_e32 v8, v161
	v_cvt_pk_fp8_f32 v8, v5, v14
	v_med3_f32 v5, v6, s49, v195
	v_med3_f32 v6, v7, s49, v195
	v_cvt_pk_fp8_f32 v9, v5, v6 op_sel:[0,0,1]
	v_pk_mul_f32 v[6:7], v[60:61], s[14:15] op_sel_hi:[1,0]
	v_cvt_pk_fp8_f32 v8, v15, v16 op_sel:[0,0,1]
	v_exp_f32_e32 v6, v6
	v_exp_f32_e32 v7, v7
	v_add_u32_e32 v5, 0x90, v4
	v_pk_mul_f32 v[12:13], v[62:63], s[14:15] op_sel_hi:[1,0]
	v_mad_i64_i32 v[10:11], s[0:1], v5, s44, v[2:3]
	v_pk_fma_f32 v[6:7], v[6:7], s[16:17], s[16:17] op_sel_hi:[1,0,0]
	v_exp_f32_e32 v12, v12
	v_rcp_f32_e32 v6, v6
	v_rcp_f32_e32 v7, v7
	v_exp_f32_e32 v13, v13
	v_lshl_add_u64 v[10:11], v[10:11], 0, v[0:1]
	global_store_dwordx2 v[10:11], v[8:9], off
	v_pk_mul_f32 v[10:11], v[60:61], v[56:57]
	v_pk_mul_f32 v[8:9], v[62:63], v[58:59]
	v_pk_mul_f32 v[6:7], v[10:11], v[6:7]
	v_pk_mul_f32 v[10:11], v[52:53], s[14:15] op_sel_hi:[1,0]
	v_med3_f32 v5, v6, s49, v195
	v_med3_f32 v14, v7, s49, v195
	v_pk_fma_f32 v[6:7], v[12:13], s[16:17], s[16:17] op_sel_hi:[1,0,0]
	v_exp_f32_e32 v10, v10
	v_rcp_f32_e32 v6, v6
	v_rcp_f32_e32 v7, v7
	v_exp_f32_e32 v11, v11
	v_pk_mul_f32 v[12:13], v[52:53], v[48:49]
	v_pk_mul_f32 v[6:7], v[8:9], v[6:7]
	v_pk_mul_f32 v[8:9], v[54:55], s[14:15] op_sel_hi:[1,0]
	v_med3_f32 v15, v6, s49, v195
	v_exp_f32_e32 v8, v8
	v_exp_f32_e32 v9, v9
	v_med3_f32 v16, v7, s49, v195
	v_pk_fma_f32 v[6:7], v[10:11], s[16:17], s[16:17] op_sel_hi:[1,0,0]
	v_pk_mul_f32 v[10:11], v[54:55], v[50:51]
	v_rcp_f32_e32 v6, v6
	v_rcp_f32_e32 v7, v7
	v_pk_fma_f32 v[8:9], v[8:9], s[16:17], s[16:17] op_sel_hi:[1,0,0]
	v_pk_mul_f32 v[6:7], v[12:13], v[6:7]
	v_rcp_f32_e32 v8, v8
	v_rcp_f32_e32 v9, v9
	v_med3_f32 v12, v6, s49, v195
	v_med3_f32 v13, v7, s49, v195
	v_pk_mul_f32 v[6:7], v[10:11], v[8:9]
	v_mov_b32_e32 v9, v161
	v_cvt_pk_fp8_f32 v9, v12, v13
	v_mov_b32_e32 v8, v161
	v_cvt_pk_fp8_f32 v8, v5, v14
	v_med3_f32 v5, v6, s49, v195
	v_med3_f32 v6, v7, s49, v195
	v_cvt_pk_fp8_f32 v9, v5, v6 op_sel:[0,0,1]
	v_pk_mul_f32 v[6:7], v[44:45], s[14:15] op_sel_hi:[1,0]
	v_cvt_pk_fp8_f32 v8, v15, v16 op_sel:[0,0,1]
	v_exp_f32_e32 v6, v6
	v_exp_f32_e32 v7, v7
	v_add_u32_e32 v5, 0xa0, v4
	v_pk_mul_f32 v[12:13], v[46:47], s[14:15] op_sel_hi:[1,0]
	v_mad_i64_i32 v[10:11], s[0:1], v5, s44, v[2:3]
	v_pk_fma_f32 v[6:7], v[6:7], s[16:17], s[16:17] op_sel_hi:[1,0,0]
	v_exp_f32_e32 v12, v12
	v_rcp_f32_e32 v6, v6
	v_rcp_f32_e32 v7, v7
	v_exp_f32_e32 v13, v13
	v_lshl_add_u64 v[10:11], v[10:11], 0, v[0:1]
	global_store_dwordx2 v[10:11], v[8:9], off
	v_pk_mul_f32 v[10:11], v[44:45], v[40:41]
	v_pk_mul_f32 v[8:9], v[46:47], v[42:43]
	v_pk_mul_f32 v[6:7], v[10:11], v[6:7]
	v_pk_mul_f32 v[10:11], v[36:37], s[14:15] op_sel_hi:[1,0]
	v_med3_f32 v5, v6, s49, v195
	v_med3_f32 v14, v7, s49, v195
	v_pk_fma_f32 v[6:7], v[12:13], s[16:17], s[16:17] op_sel_hi:[1,0,0]
	v_exp_f32_e32 v10, v10
	v_rcp_f32_e32 v6, v6
	v_rcp_f32_e32 v7, v7
	v_exp_f32_e32 v11, v11
	v_pk_mul_f32 v[12:13], v[36:37], v[32:33]
	v_add_u32_e32 v4, 0xb0, v4
	v_pk_mul_f32 v[6:7], v[8:9], v[6:7]
	v_pk_mul_f32 v[8:9], v[38:39], s[14:15] op_sel_hi:[1,0]
	v_med3_f32 v15, v6, s49, v195
	v_exp_f32_e32 v8, v8
	v_exp_f32_e32 v9, v9
	v_med3_f32 v16, v7, s49, v195
	v_pk_fma_f32 v[6:7], v[10:11], s[16:17], s[16:17] op_sel_hi:[1,0,0]
	v_pk_mul_f32 v[10:11], v[38:39], v[34:35]
	v_rcp_f32_e32 v6, v6
	v_rcp_f32_e32 v7, v7
	v_pk_fma_f32 v[8:9], v[8:9], s[16:17], s[16:17] op_sel_hi:[1,0,0]
	v_mad_i64_i32 v[2:3], s[0:1], v4, s44, v[2:3]
	v_rcp_f32_e32 v8, v8
	v_rcp_f32_e32 v9, v9
	v_pk_mul_f32 v[6:7], v[12:13], v[6:7]
	v_lshl_add_u64 v[0:1], v[2:3], 0, v[0:1]
	v_med3_f32 v12, v6, s49, v195
	v_med3_f32 v13, v7, s49, v195
	v_pk_mul_f32 v[6:7], v[10:11], v[8:9]
	v_mov_b32_e32 v8, v161
	v_mov_b32_e32 v9, v161
	v_cvt_pk_fp8_f32 v8, v5, v14
	v_cvt_pk_fp8_f32 v9, v12, v13
	v_med3_f32 v5, v6, s49, v195
	v_med3_f32 v6, v7, s49, v195
	v_cvt_pk_fp8_f32 v8, v15, v16 op_sel:[0,0,1]
	v_cvt_pk_fp8_f32 v9, v5, v6 op_sel:[0,0,1]
	s_mov_b64 s[0:1], -1
	global_store_dwordx2 v[0:1], v[8:9], off
	s_cbranch_vccnz .LBB0_1102
	s_andn2_b64 vcc, exec, s[4:5]
	s_cbranch_vccnz .LBB0_1101
	s_nop 0
	s_branch .LBB0_1101
